# removed the compiler-inserted s_waitcnt vmcnt(0) at the top of the FFN-up GEMM k-loop (it drained the LDS-DMA prefetch every iteration); plus P7/P11 load hoist
# speedup vs baseline: 1.0086x; 1.0048x over previous
.LBB0_1649:
	ds_read_b128 v[130:133], v167
	ds_read_b128 v[134:137], v167 offset:1024
	ds_read_b128 v[138:141], v167 offset:2048
	ds_read_b128 v[142:145], v167 offset:3072
	ds_read_b128 v[168:171], v228
	ds_read_b128 v[172:175], v228 offset:1024
	ds_read_b128 v[176:179], v228 offset:2048
	ds_read_b128 v[180:183], v228 offset:3072
	s_add_u32 s38, s34, 0xfff80080
	s_addc_u32 s39, s35, -1
	s_cmp_eq_u32 s77, 28
	s_cselect_b32 s45, s1, s39
	s_cselect_b32 s44, s29, s38
	s_cselect_b32 s43, s27, s47
	s_cselect_b32 s42, s41, s46
	v_lshl_add_u64 v[146:147], s[34:35], 0, v[158:159]
	s_add_i32 m0, s50, 0xc000
	ds_read_b128 v[184:187], v229
	ds_read_b128 v[188:191], v229 offset:1024
	ds_read_b128 v[192:195], v229 offset:2048
	ds_read_b128 v[196:199], v229 offset:3072
	ds_read_b128 v[200:203], v229 offset:4096
	ds_read_b128 v[204:207], v229 offset:5120
	ds_read_b128 v[208:211], v229 offset:6144
	ds_read_b128 v[212:215], v229 offset:7168
	global_load_lds_dwordx4 v[146:147], off
	v_lshl_add_u64 v[146:147], s[34:35], 0, v[160:161]
	s_add_i32 m0, s50, 0xe000
	s_nop 0
	global_load_lds_dwordx4 v[146:147], off
	s_waitcnt vmcnt(8)
	s_waitcnt lgkmcnt(0)
	s_barrier
	s_setprio 1
	s_waitcnt lgkmcnt(0)
	v_mfma_i32_16x16x64_i8 v[46:49], v[130:133], v[184:187], v[46:49]
	v_mfma_i32_16x16x64_i8 v[34:37], v[138:141], v[184:187], v[34:37]
	v_mfma_i32_16x16x64_i8 v[42:45], v[130:133], v[192:195], v[42:45]
	v_mfma_i32_16x16x64_i8 v[30:33], v[138:141], v[192:195], v[30:33]
	v_mfma_i32_16x16x64_i8 v[38:41], v[130:133], v[200:203], v[38:41]
	v_mfma_i32_16x16x64_i8 v[26:29], v[138:141], v[200:203], v[26:29]
	v_mfma_i32_16x16x64_i8 v[126:129], v[130:133], v[208:211], v[126:129]
	v_mfma_i32_16x16x64_i8 v[122:125], v[138:141], v[208:211], v[122:125]
	v_mfma_i32_16x16x64_i8 v[46:49], v[134:137], v[188:191], v[46:49]
	v_mfma_i32_16x16x64_i8 v[34:37], v[142:145], v[188:191], v[34:37]
	v_mfma_i32_16x16x64_i8 v[42:45], v[134:137], v[196:199], v[42:45]
	v_mfma_i32_16x16x64_i8 v[30:33], v[142:145], v[196:199], v[30:33]
	v_mfma_i32_16x16x64_i8 v[38:41], v[134:137], v[204:207], v[38:41]
	v_mfma_i32_16x16x64_i8 v[26:29], v[142:145], v[204:207], v[26:29]
	v_mfma_i32_16x16x64_i8 v[126:129], v[134:137], v[212:215], v[126:129]
	v_mfma_i32_16x16x64_i8 v[122:125], v[142:145], v[212:215], v[122:125]
	s_setprio 0
	s_setprio 1
	v_mfma_i32_16x16x64_i8 v[22:25], v[168:171], v[184:187], v[22:25]
	v_mfma_i32_16x16x64_i8 v[10:13], v[176:179], v[184:187], v[10:13]
	v_mfma_i32_16x16x64_i8 v[18:21], v[168:171], v[192:195], v[18:21]
	v_mfma_i32_16x16x64_i8 v[6:9], v[176:179], v[192:195], v[6:9]
	v_mfma_i32_16x16x64_i8 v[14:17], v[168:171], v[200:203], v[14:17]
	v_mfma_i32_16x16x64_i8 v[2:5], v[176:179], v[200:203], v[2:5]
	v_mfma_i32_16x16x64_i8 v[118:121], v[168:171], v[208:211], v[118:121]
	v_mfma_i32_16x16x64_i8 v[114:117], v[176:179], v[208:211], v[114:117]
	v_mfma_i32_16x16x64_i8 v[22:25], v[172:175], v[188:191], v[22:25]
	v_mfma_i32_16x16x64_i8 v[10:13], v[180:183], v[188:191], v[10:13]
	v_mfma_i32_16x16x64_i8 v[18:21], v[172:175], v[196:199], v[18:21]
	v_mfma_i32_16x16x64_i8 v[6:9], v[180:183], v[196:199], v[6:9]
	v_mfma_i32_16x16x64_i8 v[14:17], v[172:175], v[204:207], v[14:17]
	v_mfma_i32_16x16x64_i8 v[2:5], v[180:183], v[204:207], v[2:5]
	v_mfma_i32_16x16x64_i8 v[118:121], v[172:175], v[212:215], v[118:121]
	v_mfma_i32_16x16x64_i8 v[114:117], v[180:183], v[212:215], v[114:117]
	s_setprio 0
	s_barrier
	s_add_i32 s38, s64, s49
	v_lshl_add_u64 v[146:147], s[42:43], 0, v[150:151]
	s_mov_b32 m0, s38
	ds_read_b128 v[184:187], v229 offset:16384
	ds_read_b128 v[188:191], v229 offset:17408
	ds_read_b128 v[192:195], v229 offset:18432
	ds_read_b128 v[196:199], v229 offset:19456
	ds_read_b128 v[200:203], v229 offset:20480
	ds_read_b128 v[204:207], v229 offset:21504
	ds_read_b128 v[208:211], v229 offset:22528
	ds_read_b128 v[212:215], v229 offset:23552
	global_load_lds_dwordx4 v[146:147], off
	s_add_i32 m0, s38, 0x2000
	s_add_u32 s38, s42, 0x80000
	v_lshl_add_u64 v[216:217], s[42:43], 0, v[154:155]
	s_addc_u32 s39, s43, 0
	s_add_i32 s78, s65, s49
	global_load_lds_dwordx4 v[216:217], off
	v_lshl_add_u64 v[218:219], s[38:39], 0, v[150:151]
	s_mov_b32 m0, s78
	v_lshl_add_u64 v[220:221], s[44:45], 0, v[152:153]
	global_load_lds_dwordx4 v[218:219], off
	v_lshl_add_u64 v[218:219], s[38:39], 0, v[154:155]
	s_add_i32 m0, s78, 0x2000
	s_nop 0
	global_load_lds_dwordx4 v[218:219], off
	v_lshl_add_u64 v[218:219], s[44:45], 0, v[148:149]
	s_mov_b32 m0, s50
	s_nop 0
	global_load_lds_dwordx4 v[218:219], off
	s_mov_b32 m0, s51
	s_nop 0
	global_load_lds_dwordx4 v[220:221], off
	s_waitcnt vmcnt(8)
	s_waitcnt lgkmcnt(0)
	s_barrier
	s_setprio 1
	s_waitcnt lgkmcnt(0)
	v_mfma_i32_16x16x64_i8 v[94:97], v[130:133], v[184:187], v[94:97]
	v_mfma_i32_16x16x64_i8 v[70:73], v[138:141], v[184:187], v[70:73]
	v_mfma_i32_16x16x64_i8 v[86:89], v[130:133], v[192:195], v[86:89]
	v_mfma_i32_16x16x64_i8 v[62:65], v[138:141], v[192:195], v[62:65]
	v_mfma_i32_16x16x64_i8 v[78:81], v[130:133], v[200:203], v[78:81]
	v_mfma_i32_16x16x64_i8 v[54:57], v[138:141], v[200:203], v[54:57]
	v_mfma_i32_16x16x64_i8 v[110:113], v[130:133], v[208:211], v[110:113]
	v_mfma_i32_16x16x64_i8 v[106:109], v[138:141], v[208:211], v[106:109]
	v_mfma_i32_16x16x64_i8 v[94:97], v[134:137], v[188:191], v[94:97]
	v_mfma_i32_16x16x64_i8 v[70:73], v[142:145], v[188:191], v[70:73]
	v_mfma_i32_16x16x64_i8 v[86:89], v[134:137], v[196:199], v[86:89]
	v_mfma_i32_16x16x64_i8 v[62:65], v[142:145], v[196:199], v[62:65]
	v_mfma_i32_16x16x64_i8 v[78:81], v[134:137], v[204:207], v[78:81]
	v_mfma_i32_16x16x64_i8 v[54:57], v[142:145], v[204:207], v[54:57]
	v_mfma_i32_16x16x64_i8 v[110:113], v[134:137], v[212:215], v[110:113]
	v_mfma_i32_16x16x64_i8 v[106:109], v[142:145], v[212:215], v[106:109]
	s_setprio 0
	s_setprio 1
	v_mfma_i32_16x16x64_i8 v[90:93], v[168:171], v[184:187], v[90:93]
	v_mfma_i32_16x16x64_i8 v[66:69], v[176:179], v[184:187], v[66:69]
	v_mfma_i32_16x16x64_i8 v[82:85], v[168:171], v[192:195], v[82:85]
	v_mfma_i32_16x16x64_i8 v[58:61], v[176:179], v[192:195], v[58:61]
	v_mfma_i32_16x16x64_i8 v[74:77], v[168:171], v[200:203], v[74:77]
	v_mfma_i32_16x16x64_i8 v[50:53], v[176:179], v[200:203], v[50:53]
	v_mfma_i32_16x16x64_i8 v[102:105], v[168:171], v[208:211], v[102:105]
	v_mfma_i32_16x16x64_i8 v[98:101], v[176:179], v[208:211], v[98:101]
	v_mfma_i32_16x16x64_i8 v[90:93], v[172:175], v[188:191], v[90:93]
	v_mfma_i32_16x16x64_i8 v[66:69], v[180:183], v[188:191], v[66:69]
	v_mfma_i32_16x16x64_i8 v[82:85], v[172:175], v[196:199], v[82:85]
	v_mfma_i32_16x16x64_i8 v[58:61], v[180:183], v[196:199], v[58:61]
	v_mfma_i32_16x16x64_i8 v[74:77], v[172:175], v[204:207], v[74:77]
	v_mfma_i32_16x16x64_i8 v[50:53], v[180:183], v[204:207], v[50:53]
	v_mfma_i32_16x16x64_i8 v[102:105], v[172:175], v[212:215], v[102:105]
	v_mfma_i32_16x16x64_i8 v[98:101], v[180:183], v[212:215], v[98:101]
	s_setprio 0
	s_barrier
	s_add_i32 s78, 0, 0x18000
	s_add_i32 s79, 0, 0x1c000
	v_add_u32_e32 v142, s78, v1
	v_add_u32_e32 v156, s79, v1
	ds_read_b128 v[130:133], v142
	ds_read_b128 v[134:137], v142 offset:1024
	ds_read_b128 v[138:141], v142 offset:2048
	ds_read_b128 v[142:145], v142 offset:3072
	ds_read_b128 v[168:171], v156
	ds_read_b128 v[172:175], v156 offset:1024
	ds_read_b128 v[176:179], v156 offset:2048
	ds_read_b128 v[180:183], v156 offset:3072
	s_add_u32 s38, s44, 0x80000
	s_addc_u32 s39, s45, 0
	s_mov_b32 m0, s52
	v_lshl_add_u64 v[222:223], s[38:39], 0, v[148:149]
	ds_read_b128 v[184:187], v229 offset:32768
	ds_read_b128 v[188:191], v229 offset:33792
	ds_read_b128 v[192:195], v229 offset:34816
	ds_read_b128 v[196:199], v229 offset:35840
	ds_read_b128 v[200:203], v229 offset:36864
	ds_read_b128 v[204:207], v229 offset:37888
	ds_read_b128 v[208:211], v229 offset:38912
	ds_read_b128 v[212:215], v229 offset:39936
	global_load_lds_dwordx4 v[222:223], off
	v_lshl_add_u64 v[222:223], s[38:39], 0, v[152:153]
	s_mov_b32 m0, s53
	s_nop 0
	global_load_lds_dwordx4 v[222:223], off
	s_waitcnt vmcnt(8)
	s_waitcnt lgkmcnt(0)
	s_barrier
	s_setprio 1
	s_waitcnt lgkmcnt(0)
	v_mfma_i32_16x16x64_i8 v[46:49], v[130:133], v[184:187], v[46:49]
	v_mfma_i32_16x16x64_i8 v[34:37], v[138:141], v[184:187], v[34:37]
	v_mfma_i32_16x16x64_i8 v[42:45], v[130:133], v[192:195], v[42:45]
	v_mfma_i32_16x16x64_i8 v[30:33], v[138:141], v[192:195], v[30:33]
	v_mfma_i32_16x16x64_i8 v[38:41], v[130:133], v[200:203], v[38:41]
	v_mfma_i32_16x16x64_i8 v[26:29], v[138:141], v[200:203], v[26:29]
	v_mfma_i32_16x16x64_i8 v[126:129], v[130:133], v[208:211], v[126:129]
	v_mfma_i32_16x16x64_i8 v[122:125], v[138:141], v[208:211], v[122:125]
	v_mfma_i32_16x16x64_i8 v[46:49], v[134:137], v[188:191], v[46:49]
	v_mfma_i32_16x16x64_i8 v[34:37], v[142:145], v[188:191], v[34:37]
	v_mfma_i32_16x16x64_i8 v[42:45], v[134:137], v[196:199], v[42:45]
	v_mfma_i32_16x16x64_i8 v[30:33], v[142:145], v[196:199], v[30:33]
	v_mfma_i32_16x16x64_i8 v[38:41], v[134:137], v[204:207], v[38:41]
	v_mfma_i32_16x16x64_i8 v[26:29], v[142:145], v[204:207], v[26:29]
	v_mfma_i32_16x16x64_i8 v[126:129], v[134:137], v[212:215], v[126:129]
	v_mfma_i32_16x16x64_i8 v[122:125], v[142:145], v[212:215], v[122:125]
	s_setprio 0
	s_setprio 1
	v_mfma_i32_16x16x64_i8 v[22:25], v[168:171], v[184:187], v[22:25]
	v_mfma_i32_16x16x64_i8 v[10:13], v[176:179], v[184:187], v[10:13]
	v_mfma_i32_16x16x64_i8 v[18:21], v[168:171], v[192:195], v[18:21]
	v_mfma_i32_16x16x64_i8 v[6:9], v[176:179], v[192:195], v[6:9]
	v_mfma_i32_16x16x64_i8 v[14:17], v[168:171], v[200:203], v[14:17]
	v_mfma_i32_16x16x64_i8 v[2:5], v[176:179], v[200:203], v[2:5]
	v_mfma_i32_16x16x64_i8 v[118:121], v[168:171], v[208:211], v[118:121]
	v_mfma_i32_16x16x64_i8 v[114:117], v[176:179], v[208:211], v[114:117]
	v_mfma_i32_16x16x64_i8 v[22:25], v[172:175], v[188:191], v[22:25]
	v_mfma_i32_16x16x64_i8 v[10:13], v[180:183], v[188:191], v[10:13]
	v_mfma_i32_16x16x64_i8 v[18:21], v[172:175], v[196:199], v[18:21]
	v_mfma_i32_16x16x64_i8 v[6:9], v[180:183], v[196:199], v[6:9]
	v_mfma_i32_16x16x64_i8 v[14:17], v[172:175], v[204:207], v[14:17]
	v_mfma_i32_16x16x64_i8 v[2:5], v[180:183], v[204:207], v[2:5]
	v_mfma_i32_16x16x64_i8 v[118:121], v[172:175], v[212:215], v[118:121]
	v_mfma_i32_16x16x64_i8 v[114:117], v[180:183], v[212:215], v[114:117]
	s_setprio 0
	s_barrier
	s_add_i32 s38, s78, s49
	v_lshl_add_u64 v[146:147], v[146:147], 0, s[14:15]
	s_mov_b32 m0, s38
	ds_read_b128 v[184:187], v229 offset:49152
	ds_read_b128 v[188:191], v229 offset:50176
	ds_read_b128 v[192:195], v229 offset:51200
	ds_read_b128 v[196:199], v229 offset:52224
	ds_read_b128 v[200:203], v229 offset:53248
	ds_read_b128 v[204:207], v229 offset:54272
	ds_read_b128 v[208:211], v229 offset:55296
	ds_read_b128 v[212:215], v229 offset:56320
	global_load_lds_dwordx4 v[146:147], off
	s_add_i32 m0, s38, 0x2000
	s_add_u32 s38, s42, 0x80080
	v_lshl_add_u64 v[146:147], v[216:217], 0, s[14:15]
	s_addc_u32 s39, s43, 0
	s_add_i32 s42, s79, s49
	global_load_lds_dwordx4 v[146:147], off
	v_lshl_add_u64 v[146:147], s[38:39], 0, v[150:151]
	s_mov_b32 m0, s42
	s_nop 0
	global_load_lds_dwordx4 v[146:147], off
	v_lshl_add_u64 v[146:147], s[38:39], 0, v[154:155]
	s_add_i32 m0, s42, 0x2000
	s_nop 0
	global_load_lds_dwordx4 v[146:147], off
	v_lshl_add_u64 v[146:147], v[218:219], 0, s[14:15]
	s_mov_b32 m0, s57
	s_nop 0
	global_load_lds_dwordx4 v[146:147], off
	v_lshl_add_u64 v[146:147], v[220:221], 0, s[14:15]
	s_mov_b32 m0, s58
	s_nop 0
	global_load_lds_dwordx4 v[146:147], off
	s_waitcnt vmcnt(8)
	s_waitcnt lgkmcnt(0)
	s_barrier
	s_setprio 1
	s_waitcnt lgkmcnt(0)
	v_mfma_i32_16x16x64_i8 v[94:97], v[130:133], v[184:187], v[94:97]
	v_mfma_i32_16x16x64_i8 v[70:73], v[138:141], v[184:187], v[70:73]
	v_mfma_i32_16x16x64_i8 v[86:89], v[130:133], v[192:195], v[86:89]
	v_mfma_i32_16x16x64_i8 v[62:65], v[138:141], v[192:195], v[62:65]
	v_mfma_i32_16x16x64_i8 v[78:81], v[130:133], v[200:203], v[78:81]
	v_mfma_i32_16x16x64_i8 v[54:57], v[138:141], v[200:203], v[54:57]
	v_mfma_i32_16x16x64_i8 v[110:113], v[130:133], v[208:211], v[110:113]
	v_mfma_i32_16x16x64_i8 v[106:109], v[138:141], v[208:211], v[106:109]
	v_mfma_i32_16x16x64_i8 v[94:97], v[134:137], v[188:191], v[94:97]
	v_mfma_i32_16x16x64_i8 v[70:73], v[142:145], v[188:191], v[70:73]
	v_mfma_i32_16x16x64_i8 v[86:89], v[134:137], v[196:199], v[86:89]
	v_mfma_i32_16x16x64_i8 v[62:65], v[142:145], v[196:199], v[62:65]
	v_mfma_i32_16x16x64_i8 v[78:81], v[134:137], v[204:207], v[78:81]
	v_mfma_i32_16x16x64_i8 v[54:57], v[142:145], v[204:207], v[54:57]
	v_mfma_i32_16x16x64_i8 v[110:113], v[134:137], v[212:215], v[110:113]
	v_mfma_i32_16x16x64_i8 v[106:109], v[142:145], v[212:215], v[106:109]
	s_setprio 0
	s_setprio 1
	v_mfma_i32_16x16x64_i8 v[90:93], v[168:171], v[184:187], v[90:93]
	v_mfma_i32_16x16x64_i8 v[66:69], v[176:179], v[184:187], v[66:69]
	v_mfma_i32_16x16x64_i8 v[82:85], v[168:171], v[192:195], v[82:85]
	v_mfma_i32_16x16x64_i8 v[58:61], v[176:179], v[192:195], v[58:61]
	v_mfma_i32_16x16x64_i8 v[74:77], v[168:171], v[200:203], v[74:77]
	v_mfma_i32_16x16x64_i8 v[50:53], v[176:179], v[200:203], v[50:53]
	v_mfma_i32_16x16x64_i8 v[102:105], v[168:171], v[208:211], v[102:105]
	v_mfma_i32_16x16x64_i8 v[98:101], v[176:179], v[208:211], v[98:101]
	v_mfma_i32_16x16x64_i8 v[90:93], v[172:175], v[188:191], v[90:93]
	v_mfma_i32_16x16x64_i8 v[66:69], v[180:183], v[188:191], v[66:69]
	v_mfma_i32_16x16x64_i8 v[82:85], v[172:175], v[196:199], v[82:85]
	v_mfma_i32_16x16x64_i8 v[58:61], v[180:183], v[196:199], v[58:61]
	v_mfma_i32_16x16x64_i8 v[74:77], v[172:175], v[204:207], v[74:77]
	v_mfma_i32_16x16x64_i8 v[50:53], v[180:183], v[204:207], v[50:53]
	v_mfma_i32_16x16x64_i8 v[102:105], v[172:175], v[212:215], v[102:105]
	v_mfma_i32_16x16x64_i8 v[98:101], v[180:183], v[212:215], v[98:101]
	s_setprio 0
	s_barrier
	s_add_i32 s77, s77, 2
	s_add_u32 s34, s34, 0x100
	s_addc_u32 s35, s35, 0
	s_add_u32 s46, s46, 0x100
	s_addc_u32 s47, s47, 0
	s_cmp_gt_u32 s77, 29
	s_cbranch_scc0 .LBB0_1649
	s_and_b64 vcc, exec, s[16:17]
	s_cbranch_vccz .LBB0_1652
	s_barrier
